# W7 + pool compute: hoist the 8 serialised s_pool scale loads before the next-item prefetch, counted wait instead of 8x vmcnt(0)
# baseline (speedup 1.0000x reference)
.LBB0_590:
	s_or_b64 exec, exec, s[0:1]
	v_and_b32_e32 v88, 15, v68
	v_bfe_u32 v69, v68, 4, 2
	v_bfe_u32 v71, v68, 2, 2
	v_or_b32_e32 v52, s25, v88
	v_and_b32_e32 v53, 48, v68
	v_lshl_or_b32 v71, v69, 3, v71
	v_mov_b32_e32 v72, s17
	v_lshlrev_b32_e32 v68, 3, v68
	v_mul_lo_u32 v52, v52, s33
	v_lshlrev_b32_e32 v69, 7, v69
	v_mad_u32_u24 v71, v71, s33, v72
	v_and_b32_e32 v68, 24, v68
	s_waitcnt lgkmcnt(0)
	s_barrier
	v_add3_u32 v52, s8, v52, v53
	v_add3_u32 v93, v71, v69, v68
	ds_read_b128 v[64:67], v52 offset:41472
	ds_read_b128 v[60:63], v52 offset:41536
	ds_read_b128 v[56:59], v52 offset:41600
	ds_read_b128 v[52:55], v52 offset:41664
	ds_read_b64_tr_b16 v[86:87], v93 offset:1152
	ds_read_b64_tr_b16 v[84:85], v93
	ds_read_b64_tr_b16 v[68:69], v93 offset:32
	ds_read_b64_tr_b16 v[94:95], v93 offset:9728
	ds_read_b64_tr_b16 v[96:97], v93 offset:10880
	ds_read_b64_tr_b16 v[98:99], v93 offset:19456
	ds_read_b64_tr_b16 v[100:101], v93 offset:20608
	ds_read_b64_tr_b16 v[102:103], v93 offset:29184
	ds_read_b64_tr_b16 v[104:105], v93 offset:30336
	v_and_or_b32 v89, v70, 12, s25
	ds_read_b64_tr_b16 v[70:71], v93 offset:1184
	ds_read_b64_tr_b16 v[72:73], v93 offset:9760
	ds_read_b64_tr_b16 v[74:75], v93 offset:10912
	ds_read_b64_tr_b16 v[76:77], v93 offset:19488
	ds_read_b64_tr_b16 v[78:79], v93 offset:20640
	ds_read_b64_tr_b16 v[80:81], v93 offset:29216
	ds_read_b64_tr_b16 v[82:83], v93 offset:30368
	s_lshr_b32 s0, s34, 25
	s_add_i32 s0, s31, s0
	s_lshl_b32 s0, s0, 5
	s_and_b32 s0, s0, 0xfffff000
	s_add_i32 s22, s5, s0
	s_lshl_b32 s20, s4, 7
	s_ashr_i32 s23, s22, 31
	s_add_i32 s0, s20, s24
	s_lshl_b64 s[22:23], s[22:23], 12
	s_ashr_i32 s21, s20, 31
	v_readlane_b32 s4, v253, 35
	v_readlane_b32 s5, v253, 36
	s_load_dwordx16 s[36:51], s[4:5], 0x40
	s_waitcnt lgkmcnt(0)
	v_mfma_f32_16x16x32_bf16 v[84:87], v[64:67], v[84:87], 0
	v_or_b32_e32 v90, s0, v88
	v_ashrrev_i32_e32 v91, 31, v90
	s_add_u32 s1, s2, s22
	v_lshl_add_u64 v[90:91], v[90:91], 2, s[40:41]
	v_mfma_f32_16x16x32_bf16 v[84:87], v[60:63], v[94:97], v[84:87]
	s_nop 0
	s_addc_u32 s22, s3, s23
	s_lshl_b64 s[4:5], s[20:21], 1
	v_mfma_f32_16x16x32_bf16 v[84:87], v[56:59], v[98:101], v[84:87]
	s_add_u32 s1, s1, s4
	s_addc_u32 s4, s22, s5
	s_add_u32 s20, s1, 0x31000600
	v_mfma_f32_16x16x32_bf16 v[84:87], v[52:55], v[102:105], v[84:87]
	v_lshlrev_b32_e32 v89, 11, v89
	s_addc_u32 s21, s4, 0
	v_or_b32_e32 v212, v89, v88
	v_or_b32_e32 v94, 0x800, v89
	s_cmpk_gt_i32 s30, 0x1ff
	s_cbranch_scc1 .Lpool_sp_w0
	s_waitcnt vmcnt(12)
	s_branch .Lpool_sp_w1

.Lpool_sp_w1:
	s_nop 2
	v_mul_f32_e32 v84, v116, v84
	v_bfe_u32 v90, v84, 16, 1
	v_add3_u32 v84, v84, v90, s14
	v_lshl_add_u64 v[90:91], v[212:213], 1, s[20:21]
	global_store_short_d16_hi v[90:91], v84, off
	v_mul_f32_e32 v84, v116, v85
	v_bfe_u32 v85, v84, 16, 1
	v_or_b32_e32 v212, v94, v88
	v_add3_u32 v95, v84, v85, s14
	v_lshl_add_u64 v[84:85], v[212:213], 1, s[20:21]
	global_store_short_d16_hi v[84:85], v95, off
	v_mul_f32_e32 v84, v116, v86
	v_or_b32_e32 v95, 0x1000, v89
	v_bfe_u32 v85, v84, 16, 1
	v_or_b32_e32 v212, v95, v88
	v_add3_u32 v86, v84, v85, s14
	v_lshl_add_u64 v[84:85], v[212:213], 1, s[20:21]
	global_store_short_d16_hi v[84:85], v86, off
	v_mul_f32_e32 v84, v116, v87
	v_or_b32_e32 v96, 0x1800, v89
	v_bfe_u32 v85, v84, 16, 1
	v_or_b32_e32 v212, v96, v88
	v_add3_u32 v86, v84, v85, s14
	v_lshl_add_u64 v[84:85], v[212:213], 1, s[20:21]
	global_store_short_d16_hi v[84:85], v86, off
	ds_read_b64_tr_b16 v[84:85], v93 offset:64
	ds_read_b64_tr_b16 v[86:87], v93 offset:1216
	ds_read_b64_tr_b16 v[98:99], v93 offset:9792
	ds_read_b64_tr_b16 v[100:101], v93 offset:10944
	ds_read_b64_tr_b16 v[102:103], v93 offset:19520
	ds_read_b64_tr_b16 v[104:105], v93 offset:20672
	ds_read_b64_tr_b16 v[106:107], v93 offset:29248
	ds_read_b64_tr_b16 v[108:109], v93 offset:30400
	v_mfma_f32_16x16x32_bf16 v[68:71], v[64:67], v[68:71], 0
	s_ashr_i32 s1, s0, 31
	v_mov_b32_e32 v89, v213
	v_mfma_f32_16x16x32_bf16 v[68:71], v[60:63], v[72:75], v[68:71]
	v_or_b32_e32 v74, 16, v88
	v_or_b32_e32 v212, v94, v74
	v_mfma_f32_16x16x32_bf16 v[68:71], v[56:59], v[76:79], v[68:71]
	v_mfma_f32_16x16x32_bf16 v[70:73], v[52:55], v[80:83], v[68:71]
	s_nop 6
	v_lshl_add_u64 v[68:69], v[88:89], 0, s[0:1]
	v_lshl_add_u64 v[68:69], v[68:69], 2, s[40:41]
	s_nop 0
	s_nop 1
	v_mul_f32_e32 v70, v117, v70
	v_bfe_u32 v76, v70, 16, 1
	v_add3_u32 v70, v70, v76, s14
	global_store_short_d16_hi v[90:91], v70, off offset:32
	v_mul_f32_e32 v70, v117, v71
	v_bfe_u32 v71, v70, 16, 1
	v_add3_u32 v76, v70, v71, s14
	v_lshl_add_u64 v[70:71], v[212:213], 1, s[20:21]
	global_store_short_d16_hi v[70:71], v76, off
	v_mul_f32_e32 v70, v117, v72
	v_bfe_u32 v71, v70, 16, 1
	v_or_b32_e32 v212, v95, v74
	v_add3_u32 v72, v70, v71, s14
	v_lshl_add_u64 v[70:71], v[212:213], 1, s[20:21]
	global_store_short_d16_hi v[70:71], v72, off
	v_mul_f32_e32 v70, v117, v73
	v_bfe_u32 v71, v70, 16, 1
	v_or_b32_e32 v212, v96, v74
	v_add3_u32 v72, v70, v71, s14
	v_lshl_add_u64 v[70:71], v[212:213], 1, s[20:21]
	global_store_short_d16_hi v[70:71], v72, off
	ds_read_b64_tr_b16 v[70:71], v93 offset:96
	ds_read_b64_tr_b16 v[72:73], v93 offset:1248
	ds_read_b64_tr_b16 v[74:75], v93 offset:9824
	ds_read_b64_tr_b16 v[76:77], v93 offset:10976
	ds_read_b64_tr_b16 v[78:79], v93 offset:19552
	ds_read_b64_tr_b16 v[80:81], v93 offset:20704
	ds_read_b64_tr_b16 v[110:111], v93 offset:29280
	ds_read_b64_tr_b16 v[112:113], v93 offset:30432
	s_waitcnt lgkmcnt(14)
	v_mfma_f32_16x16x32_bf16 v[82:85], v[64:67], v[84:87], 0
	s_nop 0
	v_or_b32_e32 v86, 32, v88
	v_or_b32_e32 v212, v94, v86
	s_waitcnt lgkmcnt(12)
	v_mfma_f32_16x16x32_bf16 v[82:85], v[60:63], v[98:101], v[82:85]
	s_waitcnt lgkmcnt(10)
	v_mfma_f32_16x16x32_bf16 v[82:85], v[56:59], v[102:105], v[82:85]
	s_waitcnt lgkmcnt(8)
	v_mfma_f32_16x16x32_bf16 v[82:85], v[52:55], v[106:109], v[82:85]
	s_nop 1
	s_nop 6
	v_mul_f32_e32 v82, v118, v82
	v_bfe_u32 v89, v82, 16, 1
	v_add3_u32 v82, v82, v89, s14
	global_store_short_d16_hi v[90:91], v82, off offset:64
	v_mul_f32_e32 v82, v118, v83
	v_bfe_u32 v83, v82, 16, 1
	v_add3_u32 v89, v82, v83, s14
	v_lshl_add_u64 v[82:83], v[212:213], 1, s[20:21]
	global_store_short_d16_hi v[82:83], v89, off
	v_mul_f32_e32 v82, v118, v84
	v_bfe_u32 v83, v82, 16, 1
	v_or_b32_e32 v212, v95, v86
	v_add3_u32 v84, v82, v83, s14
	v_lshl_add_u64 v[82:83], v[212:213], 1, s[20:21]
	global_store_short_d16_hi v[82:83], v84, off
	v_mul_f32_e32 v82, v118, v85
	v_bfe_u32 v83, v82, 16, 1
	v_or_b32_e32 v212, v96, v86
	v_add3_u32 v84, v82, v83, s14
	v_lshl_add_u64 v[82:83], v[212:213], 1, s[20:21]
	global_store_short_d16_hi v[82:83], v84, off
	ds_read_b64_tr_b16 v[82:83], v93 offset:128
	ds_read_b64_tr_b16 v[84:85], v93 offset:1280
	ds_read_b64_tr_b16 v[98:99], v93 offset:9856
	ds_read_b64_tr_b16 v[100:101], v93 offset:11008
	ds_read_b64_tr_b16 v[102:103], v93 offset:19584
	ds_read_b64_tr_b16 v[104:105], v93 offset:20736
	ds_read_b64_tr_b16 v[106:107], v93 offset:29312
	ds_read_b64_tr_b16 v[108:109], v93 offset:30464
	s_waitcnt lgkmcnt(14)
	v_mfma_f32_16x16x32_bf16 v[70:73], v[64:67], v[70:73], 0
	s_waitcnt lgkmcnt(12)
	v_mfma_f32_16x16x32_bf16 v[70:73], v[60:63], v[74:77], v[70:73]
	s_nop 0
	v_or_b32_e32 v74, 48, v88
	v_or_b32_e32 v212, v94, v74
	s_waitcnt lgkmcnt(10)
	v_mfma_f32_16x16x32_bf16 v[70:73], v[56:59], v[78:81], v[70:73]
	s_waitcnt lgkmcnt(8)
	v_mfma_f32_16x16x32_bf16 v[70:73], v[52:55], v[110:113], v[70:73]
	s_nop 1
	s_nop 6
	v_mul_f32_e32 v70, v119, v70
	v_bfe_u32 v76, v70, 16, 1
	v_add3_u32 v70, v70, v76, s14
	global_store_short_d16_hi v[90:91], v70, off offset:96
	v_mul_f32_e32 v70, v119, v71
	v_bfe_u32 v71, v70, 16, 1
	v_add3_u32 v76, v70, v71, s14
	v_lshl_add_u64 v[70:71], v[212:213], 1, s[20:21]
	global_store_short_d16_hi v[70:71], v76, off
	v_mul_f32_e32 v70, v119, v72
	v_bfe_u32 v71, v70, 16, 1
	v_or_b32_e32 v212, v95, v74
	v_add3_u32 v72, v70, v71, s14
	v_lshl_add_u64 v[70:71], v[212:213], 1, s[20:21]
	global_store_short_d16_hi v[70:71], v72, off
	v_mul_f32_e32 v70, v119, v73
	v_bfe_u32 v71, v70, 16, 1
	v_or_b32_e32 v212, v96, v74
	v_add3_u32 v72, v70, v71, s14
	v_lshl_add_u64 v[70:71], v[212:213], 1, s[20:21]
	global_store_short_d16_hi v[70:71], v72, off
	ds_read_b64_tr_b16 v[70:71], v93 offset:160
	ds_read_b64_tr_b16 v[72:73], v93 offset:1312
	ds_read_b64_tr_b16 v[74:75], v93 offset:9888
	ds_read_b64_tr_b16 v[76:77], v93 offset:11040
	ds_read_b64_tr_b16 v[78:79], v93 offset:19616
	ds_read_b64_tr_b16 v[80:81], v93 offset:20768
	ds_read_b64_tr_b16 v[110:111], v93 offset:29344
	ds_read_b64_tr_b16 v[112:113], v93 offset:30496
	s_nop 0
	s_waitcnt lgkmcnt(14)
	v_mfma_f32_16x16x32_bf16 v[82:85], v[64:67], v[82:85], 0
	v_or_b32_e32 v86, 64, v88
	v_or_b32_e32 v212, v94, v86
	s_waitcnt lgkmcnt(12)
	v_mfma_f32_16x16x32_bf16 v[82:85], v[60:63], v[98:101], v[82:85]
	s_waitcnt lgkmcnt(10)
	v_mfma_f32_16x16x32_bf16 v[82:85], v[56:59], v[102:105], v[82:85]
	s_waitcnt lgkmcnt(8)
	v_mfma_f32_16x16x32_bf16 v[82:85], v[52:55], v[106:109], v[82:85]
	s_nop 1
	s_nop 6
	v_mul_f32_e32 v82, v120, v82
	v_bfe_u32 v89, v82, 16, 1
	v_add3_u32 v82, v82, v89, s14
	global_store_short_d16_hi v[90:91], v82, off offset:128
	v_mul_f32_e32 v82, v120, v83
	v_bfe_u32 v83, v82, 16, 1
	v_add3_u32 v89, v82, v83, s14
	v_lshl_add_u64 v[82:83], v[212:213], 1, s[20:21]
	global_store_short_d16_hi v[82:83], v89, off
	v_mul_f32_e32 v82, v120, v84
	v_bfe_u32 v83, v82, 16, 1
	v_or_b32_e32 v212, v95, v86
	v_add3_u32 v84, v82, v83, s14
	v_lshl_add_u64 v[82:83], v[212:213], 1, s[20:21]
	global_store_short_d16_hi v[82:83], v84, off
	v_mul_f32_e32 v82, v120, v85
	v_bfe_u32 v83, v82, 16, 1
	v_or_b32_e32 v212, v96, v86
	v_add3_u32 v84, v82, v83, s14
	v_lshl_add_u64 v[82:83], v[212:213], 1, s[20:21]
	global_store_short_d16_hi v[82:83], v84, off
	ds_read_b64_tr_b16 v[82:83], v93 offset:192
	ds_read_b64_tr_b16 v[84:85], v93 offset:1344
	ds_read_b64_tr_b16 v[98:99], v93 offset:9920
	ds_read_b64_tr_b16 v[100:101], v93 offset:11072
	ds_read_b64_tr_b16 v[102:103], v93 offset:19648
	ds_read_b64_tr_b16 v[104:105], v93 offset:20800
	ds_read_b64_tr_b16 v[106:107], v93 offset:29376
	ds_read_b64_tr_b16 v[108:109], v93 offset:30528
	s_waitcnt lgkmcnt(14)
	v_mfma_f32_16x16x32_bf16 v[70:73], v[64:67], v[70:73], 0
	s_waitcnt lgkmcnt(12)
	v_mfma_f32_16x16x32_bf16 v[70:73], v[60:63], v[74:77], v[70:73]
	s_nop 0
	v_or_b32_e32 v74, 0x50, v88
	v_or_b32_e32 v212, v94, v74
	s_waitcnt lgkmcnt(10)
	v_mfma_f32_16x16x32_bf16 v[70:73], v[56:59], v[78:81], v[70:73]
	s_waitcnt lgkmcnt(8)
	v_mfma_f32_16x16x32_bf16 v[70:73], v[52:55], v[110:113], v[70:73]
	s_nop 1
	s_nop 6
	v_mul_f32_e32 v70, v121, v70
	v_bfe_u32 v76, v70, 16, 1
	v_add3_u32 v70, v70, v76, s14
	global_store_short_d16_hi v[90:91], v70, off offset:160
	v_mul_f32_e32 v70, v121, v71
	v_bfe_u32 v71, v70, 16, 1
	v_add3_u32 v76, v70, v71, s14
	v_lshl_add_u64 v[70:71], v[212:213], 1, s[20:21]
	global_store_short_d16_hi v[70:71], v76, off
	v_mul_f32_e32 v70, v121, v72
	v_bfe_u32 v71, v70, 16, 1
	v_or_b32_e32 v212, v95, v74
	v_add3_u32 v72, v70, v71, s14
	v_lshl_add_u64 v[70:71], v[212:213], 1, s[20:21]
	global_store_short_d16_hi v[70:71], v72, off
	v_mul_f32_e32 v70, v121, v73
	v_bfe_u32 v71, v70, 16, 1
	v_or_b32_e32 v212, v96, v74
	v_add3_u32 v72, v70, v71, s14
	v_lshl_add_u64 v[70:71], v[212:213], 1, s[20:21]
	global_store_short_d16_hi v[70:71], v72, off
	ds_read_b64_tr_b16 v[70:71], v93 offset:224
	ds_read_b64_tr_b16 v[72:73], v93 offset:1376
	ds_read_b64_tr_b16 v[74:75], v93 offset:9952
	ds_read_b64_tr_b16 v[76:77], v93 offset:11104
	ds_read_b64_tr_b16 v[78:79], v93 offset:19680
	ds_read_b64_tr_b16 v[80:81], v93 offset:20832
	ds_read_b64_tr_b16 v[110:111], v93 offset:29408
	ds_read_b64_tr_b16 v[112:113], v93 offset:30560
	s_nop 0
	s_waitcnt lgkmcnt(14)
	v_mfma_f32_16x16x32_bf16 v[82:85], v[64:67], v[82:85], 0
	v_or_b32_e32 v86, 0x60, v88
	v_or_b32_e32 v212, v94, v86
	s_waitcnt lgkmcnt(12)
	v_mfma_f32_16x16x32_bf16 v[82:85], v[60:63], v[98:101], v[82:85]
	s_waitcnt lgkmcnt(10)
	v_mfma_f32_16x16x32_bf16 v[82:85], v[56:59], v[102:105], v[82:85]
	s_waitcnt lgkmcnt(8)
	v_mfma_f32_16x16x32_bf16 v[82:85], v[52:55], v[106:109], v[82:85]
	s_nop 1
	s_nop 6
	v_mul_f32_e32 v82, v122, v82
	v_bfe_u32 v89, v82, 16, 1
	v_add3_u32 v82, v82, v89, s14
	global_store_short_d16_hi v[90:91], v82, off offset:192
	v_mul_f32_e32 v82, v122, v83
	v_bfe_u32 v83, v82, 16, 1
	v_add3_u32 v89, v82, v83, s14
	v_lshl_add_u64 v[82:83], v[212:213], 1, s[20:21]
	global_store_short_d16_hi v[82:83], v89, off
	v_mul_f32_e32 v82, v122, v84
	v_bfe_u32 v83, v82, 16, 1
	v_or_b32_e32 v212, v95, v86
	v_add3_u32 v84, v82, v83, s14
	v_lshl_add_u64 v[82:83], v[212:213], 1, s[20:21]
	global_store_short_d16_hi v[82:83], v84, off
	v_mul_f32_e32 v82, v122, v85
	v_bfe_u32 v83, v82, 16, 1
	v_or_b32_e32 v212, v96, v86
	v_add3_u32 v84, v82, v83, s14
	v_lshl_add_u64 v[82:83], v[212:213], 1, s[20:21]
	global_store_short_d16_hi v[82:83], v84, off
	s_nop 0
	s_waitcnt lgkmcnt(6)
	v_mfma_f32_16x16x32_bf16 v[64:67], v[64:67], v[70:73], 0
	v_or_b32_e32 v69, 0x70, v88
	v_or_b32_e32 v212, v94, v69
	s_waitcnt lgkmcnt(4)
	v_mfma_f32_16x16x32_bf16 v[60:63], v[60:63], v[74:77], v[64:67]
	s_waitcnt lgkmcnt(2)
	v_mfma_f32_16x16x32_bf16 v[56:59], v[56:59], v[78:81], v[60:63]
	s_nop 1
	v_lshl_add_u64 v[64:65], v[212:213], 1, s[20:21]
	v_or_b32_e32 v212, v95, v69
	s_waitcnt lgkmcnt(0)
	v_mfma_f32_16x16x32_bf16 v[52:55], v[52:55], v[110:113], v[56:59]
	v_lshl_add_u64 v[60:61], v[212:213], 1, s[20:21]
	v_or_b32_e32 v212, v96, v69
	v_lshl_add_u64 v[62:63], v[212:213], 1, s[20:21]
	s_nop 1
	s_nop 3
	v_mul_f32_e32 v52, v123, v52
	v_mul_f32_e32 v53, v123, v53
	v_mul_f32_e32 v54, v123, v54
	v_mul_f32_e32 v55, v123, v55
	v_bfe_u32 v56, v52, 16, 1
	v_bfe_u32 v57, v53, 16, 1
	v_bfe_u32 v58, v54, 16, 1
	v_bfe_u32 v59, v55, 16, 1
	v_add3_u32 v52, v52, v56, s14
	v_add3_u32 v53, v53, v57, s14
	v_add3_u32 v54, v54, v58, s14
	v_add3_u32 v55, v55, v59, s14
	global_store_short_d16_hi v[90:91], v52, off offset:224
	global_store_short_d16_hi v[64:65], v53, off
	global_store_short_d16_hi v[60:61], v54, off
	global_store_short_d16_hi v[62:63], v55, off
	s_waitcnt lgkmcnt(0)
	s_barrier
	s_cmpk_gt_i32 s30, 0x1ff
	s_mov_b32 s31, s30
	s_cbranch_scc1 .LBB0_618

.LBB0_601:
	s_or_b64 exec, exec, s[4:5]
	v_lshlrev_b32_e32 v52, 2, v68
	v_lshrrev_b32_e32 v61, 5, v68
	v_ashrrev_i32_e32 v62, 2, v68
	v_and_b32_e32 v53, 0x7c, v52
	v_mul_lo_u32 v61, v61, s33
	v_lshlrev_b32_e32 v62, 1, v62
	v_add_u32_e32 v61, s17, v61
	v_and_b32_e32 v62, 0xffffff80, v62
	v_lshlrev_b32_e32 v63, 1, v53
	s_waitcnt vmcnt(7)
	v_cvt_pk_bf16_f32 v58, v20, v21
	v_cvt_pk_bf16_f32 v59, v22, v23
	v_add3_u32 v61, v61, v62, v63
	ds_write_b64 v61, v[58:59]
	v_lshrrev_b32_e32 v61, 5, v54
	v_ashrrev_i32_e32 v54, 2, v54
	v_mul_lo_u32 v61, v61, s33
	v_lshlrev_b32_e32 v54, 1, v54
	v_add_u32_e32 v61, s17, v61
	v_and_b32_e32 v54, 0xffffff80, v54
	s_waitcnt vmcnt(6)
	v_cvt_pk_bf16_f32 v58, v24, v25
	v_cvt_pk_bf16_f32 v59, v26, v27
	v_add3_u32 v54, v61, v54, v63
	ds_write_b64 v54, v[58:59]
	v_lshrrev_b32_e32 v54, 5, v55
	v_ashrrev_i32_e32 v55, 2, v55
	v_mul_lo_u32 v54, v54, s33
	v_lshlrev_b32_e32 v55, 1, v55
	v_add_u32_e32 v54, s17, v54
	v_and_b32_e32 v55, 0xffffff80, v55
	s_waitcnt vmcnt(5)
	v_cvt_pk_bf16_f32 v58, v28, v29
	v_cvt_pk_bf16_f32 v59, v30, v31
	v_add3_u32 v54, v54, v55, v63
	ds_write_b64 v54, v[58:59]
	v_lshrrev_b32_e32 v58, 5, v56
	v_ashrrev_i32_e32 v56, 2, v56
	v_mul_lo_u32 v58, v58, s33
	v_lshlrev_b32_e32 v56, 1, v56
	v_add_u32_e32 v58, s17, v58
	v_and_b32_e32 v56, 0xffffff80, v56
	s_waitcnt vmcnt(4)
	v_cvt_pk_bf16_f32 v54, v32, v33
	v_cvt_pk_bf16_f32 v55, v34, v35
	v_add3_u32 v56, v58, v56, v63
	ds_write_b64 v56, v[54:55]
	v_lshrrev_b32_e32 v56, 5, v57
	v_ashrrev_i32_e32 v57, 2, v57
	v_mul_lo_u32 v56, v56, s33
	v_lshlrev_b32_e32 v57, 1, v57
	v_add_u32_e32 v56, s17, v56
	v_and_b32_e32 v57, 0xffffff80, v57
	s_waitcnt vmcnt(3)
	v_cvt_pk_bf16_f32 v54, v36, v37
	v_cvt_pk_bf16_f32 v55, v38, v39
	v_add3_u32 v56, v56, v57, v63
	ds_write_b64 v56, v[54:55]
	v_add_u32_e32 v56, 0xa00, v68
	v_lshrrev_b32_e32 v57, 5, v56
	v_ashrrev_i32_e32 v56, 2, v56
	v_mul_lo_u32 v57, v57, s33
	v_lshlrev_b32_e32 v56, 1, v56
	v_add_u32_e32 v57, s17, v57
	v_and_b32_e32 v56, 0xffffff80, v56
	s_waitcnt vmcnt(2)
	v_cvt_pk_bf16_f32 v54, v40, v41
	v_cvt_pk_bf16_f32 v55, v42, v43
	v_add3_u32 v56, v57, v56, v63
	ds_write_b64 v56, v[54:55]
	v_add_u32_e32 v56, 0xc00, v68
	v_lshrrev_b32_e32 v57, 5, v56
	v_ashrrev_i32_e32 v56, 2, v56
	v_mul_lo_u32 v57, v57, s33
	v_lshlrev_b32_e32 v56, 1, v56
	v_add_u32_e32 v57, s17, v57
	v_and_b32_e32 v56, 0xffffff80, v56
	s_waitcnt vmcnt(1)
	v_cvt_pk_bf16_f32 v54, v44, v45
	v_cvt_pk_bf16_f32 v55, v46, v47
	v_add3_u32 v56, v57, v56, v63
	ds_write_b64 v56, v[54:55]
	v_add_u32_e32 v56, 0xe00, v68
	v_lshrrev_b32_e32 v57, 5, v56
	v_ashrrev_i32_e32 v56, 2, v56
	v_mul_lo_u32 v57, v57, s33
	v_lshlrev_b32_e32 v56, 1, v56
	v_add_u32_e32 v57, s17, v57
	v_and_b32_e32 v56, 0xffffff80, v56
	s_waitcnt vmcnt(0)
	v_cvt_pk_bf16_f32 v54, v48, v49
	v_cvt_pk_bf16_f32 v55, v50, v51
	v_add3_u32 v56, v57, v56, v63
	ds_write_b64 v56, v[54:55]
	s_waitcnt lgkmcnt(0)
	s_barrier
	s_lshl_b32 s0, s35, 2
	s_sub_i32 s0, s31, s0
	s_lshl_b32 s0, s0, 7
	s_add_i32 s0, s0, s24
	v_readlane_b32 s4, v253, 35
	v_readlane_b32 s5, v253, 36
	v_and_b32_e32 v114, 15, v68
	v_or_b32_e32 v114, s0, v114
	v_ashrrev_i32_e32 v115, 31, v114
	s_load_dwordx2 s[4:5], s[4:5], 0x50
	s_waitcnt lgkmcnt(0)
	v_lshl_add_u64 v[114:115], v[114:115], 2, s[4:5]
	global_load_dword v116, v[114:115], off
	global_load_dword v117, v[114:115], off offset:64
	global_load_dword v118, v[114:115], off offset:128
	global_load_dword v119, v[114:115], off offset:192
	global_load_dword v120, v[114:115], off offset:256
	global_load_dword v121, v[114:115], off offset:320
	global_load_dword v122, v[114:115], off offset:384
	global_load_dword v123, v[114:115], off offset:448
	s_add_i32 s30, s31, s13
	s_cmpk_gt_i32 s30, 0x1ff
	s_cbranch_scc1 .LBB0_609
	s_ashr_i32 s1, s30, 31
	s_lshr_b32 s0, s1, 30
	s_add_i32 s4, s30, s0
	s_ashr_i32 s5, s4, 2
	s_and_b32 s0, s4, -4
	s_ashr_i32 s4, s4, 31
	s_lshr_b32 s1, s1, 25
	s_lshr_b32 s4, s4, 27
	s_add_i32 s1, s30, s1
	s_add_i32 s4, s5, s4
	s_ashr_i32 s1, s1, 7
	s_sub_i32 s0, s30, s0
	s_andn2_b32 s4, s4, 31
	s_lshl_b32 s1, s1, 2
	s_sub_i32 s22, s5, s4
	s_add_i32 s20, s1, s0
	s_lshl_b32 s4, s22, 7
	s_ashr_i32 s21, s20, 31
	s_ashr_i32 s5, s4, 31
	s_lshl_b64 s[20:21], s[20:21], 20
	s_add_u32 s1, s15, s20
	s_addc_u32 s20, s16, s21
	s_lshl_b64 s[4:5], s[4:5], 8
	s_add_u32 s4, s1, s4
	s_addc_u32 s5, s20, s5
	s_cmp_eq_u32 s22, 0
	s_cselect_b64 s[20:21], -1, 0
	s_and_saveexec_b64 s[22:23], vcc
	s_cbranch_execz .LBB0_614
	s_and_b64 vcc, s[42:43], s[20:21]
	v_cndmask_b32_e32 v0, 0, v218, vcc
	v_add_u32_e32 v212, v0, v60
	v_lshl_add_u64 v[0:1], v[212:213], 1, s[4:5]
	global_load_dwordx4 v[0:3], v[0:1], off
	s_or_b64 exec, exec, s[22:23]
	s_and_saveexec_b64 s[22:23], s[36:37]
	s_cbranch_execnz .LBB0_615
